# nt hint also on the P6 bf16 row stores (read again only in P10) and the P4 gate loads (read once)
# baseline (speedup 1.0000x reference)
.LBB0_829:
	s_mul_i32 s0, s65, 0x2c00
	s_mul_hi_u32 s1, s64, 0x2c00
	s_add_i32 s1, s1, s0
	s_mul_i32 s0, s64, 0x2c00
	s_add_u32 s0, s44, s0
	v_lshlrev_b32_e32 v66, 6, v148
	s_addc_u32 s1, s45, s1
	v_ashrrev_i32_e32 v67, 31, v66
	v_lshl_add_u64 v[68:69], v[66:67], 1, s[0:1]
	v_lshlrev_b32_e32 v146, 1, v195
	v_lshl_add_u64 v[76:77], v[68:69], 0, v[146:147]
	v_mul_u32_u24_e32 v70, 0x2c00, v209
	v_mov_b32_e32 v71, v147
	v_lshl_add_u64 v[70:71], v[76:77], 0, v[70:71]
	v_mul_u32_u24_e32 v68, 0xb000, v194
	v_mov_b32_e32 v69, v147
	v_add_co_u32_e32 v72, vcc, s78, v70
	v_lshl_add_u64 v[68:69], v[76:77], 0, v[68:69]
	s_nop 0
	v_addc_co_u32_e32 v73, vcc, 0, v71, vcc
	v_mad_u32_u24 v78, v209, s79, v1
	v_mov_b32_e32 v79, v147
	v_lshl_add_u64 v[74:75], v[70:71], 0, s[58:59]
	v_lshl_add_u64 v[78:79], v[76:77], 0, v[78:79]
	global_load_ushort v140, v[68:69], off nt
	s_nop 0
	global_load_ushort v68, v[68:69], off offset:64 nt
	s_nop 0
	global_load_ushort v135, v[70:71], off nt
	global_load_ushort v69, v[70:71], off offset:64 nt
	s_nop 0
	global_load_ushort v72, v[72:73], off offset:3072 nt
	s_nop 0
	global_load_ushort v73, v[78:79], off nt
	global_load_ushort v71, v[78:79], off offset:64 nt
	global_load_ushort v70, v[74:75], off offset:64 nt
	v_mad_u32_u24 v74, v209, s79, v152
	v_mov_b32_e32 v75, v147
	v_mad_u32_u24 v78, v209, s79, v153
	v_mov_b32_e32 v79, v147
	s_waitcnt vmcnt(8)
	v_mad_u32_u24 v82, v209, s79, v155
	v_mov_b32_e32 v83, v147
	v_lshl_add_u64 v[74:75], v[76:77], 0, v[74:75]
	v_lshl_add_u64 v[78:79], v[76:77], 0, v[78:79]
	v_mad_u32_u24 v80, v209, s79, v154
	v_mov_b32_e32 v81, v147
	v_lshl_add_u64 v[82:83], v[76:77], 0, v[82:83]
	v_lshl_add_u64 v[80:81], v[76:77], 0, v[80:81]
	global_load_ushort v134, v[74:75], off nt
	global_load_ushort v133, v[74:75], off offset:64 nt
	global_load_ushort v132, v[78:79], off nt
	global_load_ushort v131, v[78:79], off offset:64 nt
	global_load_ushort v130, v[80:81], off nt
	global_load_ushort v129, v[80:81], off offset:64 nt
	global_load_ushort v128, v[82:83], off nt
	global_load_ushort v74, v[82:83], off offset:64 nt
	v_mad_u32_u24 v78, v209, s79, v156
	v_mov_b32_e32 v79, v147
	v_mad_u32_u24 v82, v209, s79, v158
	v_mov_b32_e32 v83, v147
	v_mad_u32_u24 v84, v209, s79, v159
	v_mov_b32_e32 v85, v147
	v_lshl_add_u64 v[78:79], v[76:77], 0, v[78:79]
	v_mad_u32_u24 v80, v209, s79, v157
	v_mov_b32_e32 v81, v147
	v_lshl_add_u64 v[82:83], v[76:77], 0, v[82:83]
	v_lshl_add_u64 v[84:85], v[76:77], 0, v[84:85]
	v_lshl_add_u64 v[80:81], v[76:77], 0, v[80:81]
	global_load_ushort v127, v[78:79], off nt
	global_load_ushort v126, v[78:79], off offset:64 nt
	global_load_ushort v125, v[80:81], off nt
	global_load_ushort v124, v[80:81], off offset:64 nt
	global_load_ushort v123, v[82:83], off nt
	global_load_ushort v122, v[82:83], off offset:64 nt
	global_load_ushort v121, v[84:85], off nt
	global_load_ushort v75, v[84:85], off offset:64 nt
	v_mad_u32_u24 v78, v209, s79, v160
	v_mov_b32_e32 v79, v147
	v_mad_u32_u24 v82, v209, s79, v162
	v_mov_b32_e32 v83, v147
	v_mad_u32_u24 v84, v209, s79, v163
	v_mov_b32_e32 v85, v147
	v_lshl_add_u64 v[78:79], v[76:77], 0, v[78:79]
	v_mad_u32_u24 v80, v209, s79, v161
	v_mov_b32_e32 v81, v147
	v_lshl_add_u64 v[82:83], v[76:77], 0, v[82:83]
	v_lshl_add_u64 v[84:85], v[76:77], 0, v[84:85]
	v_lshl_add_u64 v[80:81], v[76:77], 0, v[80:81]
	global_load_ushort v120, v[78:79], off nt
	global_load_ushort v119, v[78:79], off offset:64 nt
	global_load_ushort v118, v[80:81], off nt
	global_load_ushort v117, v[80:81], off offset:64 nt
	global_load_ushort v116, v[82:83], off nt
	global_load_ushort v115, v[82:83], off offset:64 nt
	global_load_ushort v114, v[84:85], off nt
	global_load_ushort v113, v[84:85], off offset:64 nt
	v_mad_u32_u24 v78, v209, s79, v164
	v_mov_b32_e32 v79, v147
	v_mad_u32_u24 v82, v209, s79, v166
	v_mov_b32_e32 v83, v147
	v_mad_u32_u24 v84, v209, s79, v167
	v_mov_b32_e32 v85, v147
	v_lshl_add_u64 v[78:79], v[76:77], 0, v[78:79]
	v_mad_u32_u24 v80, v209, s79, v165
	v_mov_b32_e32 v81, v147
	v_lshl_add_u64 v[82:83], v[76:77], 0, v[82:83]
	v_lshl_add_u64 v[84:85], v[76:77], 0, v[84:85]
	v_lshl_add_u64 v[80:81], v[76:77], 0, v[80:81]
	global_load_ushort v112, v[78:79], off nt
	global_load_ushort v111, v[78:79], off offset:64 nt
	global_load_ushort v110, v[80:81], off nt
	global_load_ushort v109, v[80:81], off offset:64 nt
	global_load_ushort v108, v[82:83], off nt
	global_load_ushort v107, v[82:83], off offset:64 nt
	global_load_ushort v106, v[84:85], off nt
	global_load_ushort v105, v[84:85], off offset:64 nt
	v_mad_u32_u24 v78, v209, s79, v168
	v_mov_b32_e32 v79, v147
	v_mad_u32_u24 v82, v209, s79, v170
	v_mov_b32_e32 v83, v147
	v_mad_u32_u24 v84, v209, s79, v171
	v_mov_b32_e32 v85, v147
	v_lshl_add_u64 v[78:79], v[76:77], 0, v[78:79]
	v_mad_u32_u24 v80, v209, s79, v169
	v_mov_b32_e32 v81, v147
	v_lshl_add_u64 v[82:83], v[76:77], 0, v[82:83]
	v_lshl_add_u64 v[84:85], v[76:77], 0, v[84:85]
	v_lshl_add_u64 v[80:81], v[76:77], 0, v[80:81]
	global_load_ushort v104, v[78:79], off nt
	global_load_ushort v103, v[78:79], off offset:64 nt
	global_load_ushort v102, v[80:81], off nt
	global_load_ushort v101, v[80:81], off offset:64 nt
	global_load_ushort v100, v[82:83], off nt
	global_load_ushort v99, v[82:83], off offset:64 nt
	global_load_ushort v98, v[84:85], off nt
	s_nop 0
	global_load_ushort v85, v[84:85], off offset:64 nt
	v_mad_u32_u24 v78, v209, s79, v172
	v_mov_b32_e32 v79, v147
	v_mad_u32_u24 v82, v209, s79, v174
	v_mov_b32_e32 v83, v147
	v_lshl_add_u64 v[78:79], v[76:77], 0, v[78:79]
	v_mad_u32_u24 v80, v209, s79, v173
	v_mov_b32_e32 v81, v147
	v_lshl_add_u64 v[82:83], v[76:77], 0, v[82:83]
	v_mad_u32_u24 v86, v209, s79, v175
	v_mov_b32_e32 v87, v147
	v_lshl_add_u64 v[80:81], v[76:77], 0, v[80:81]
	v_lshl_add_u64 v[86:87], v[76:77], 0, v[86:87]
	global_load_ushort v97, v[78:79], off nt
	global_load_ushort v96, v[78:79], off offset:64 nt
	global_load_ushort v95, v[80:81], off nt
	global_load_ushort v94, v[80:81], off offset:64 nt
	global_load_ushort v93, v[82:83], off nt
	global_load_ushort v92, v[82:83], off offset:64 nt
	global_load_ushort v91, v[86:87], off nt
	global_load_ushort v90, v[86:87], off offset:64 nt
	v_mad_u32_u24 v78, v209, s79, v176
	v_mov_b32_e32 v79, v147
	v_mad_u32_u24 v82, v209, s79, v178
	v_mov_b32_e32 v83, v147
	v_lshl_add_u64 v[78:79], v[76:77], 0, v[78:79]
	v_mad_u32_u24 v80, v209, s79, v177
	v_mov_b32_e32 v81, v147
	v_lshl_add_u64 v[136:137], v[76:77], 0, v[82:83]
	v_mad_u32_u24 v82, v209, s79, v179
	v_lshl_add_u64 v[80:81], v[76:77], 0, v[80:81]
	v_lshl_add_u64 v[138:139], v[76:77], 0, v[82:83]
	global_load_ushort v89, v[78:79], off nt
	global_load_ushort v88, v[78:79], off offset:64 nt
	global_load_ushort v87, v[80:81], off nt
	global_load_ushort v86, v[80:81], off offset:64 nt
	global_load_ushort v82, v[136:137], off nt
	s_nop 0
	global_load_ushort v79, v[136:137], off offset:64 nt
	global_load_ushort v77, v[138:139], off nt
	global_load_ushort v76, v[138:139], off offset:64 nt
	v_and_b32_e32 v80, 64, v212
	v_add_u32_e32 v83, 64, v80
	s_waitcnt vmcnt(62)
	v_lshlrev_b32_e32 v80, 16, v140
	v_mul_f32_e32 v81, 0xbfb8aa3b, v80
	v_lshlrev_b32_e32 v84, 16, v68
	v_exp_f32_e32 v81, v81
	v_mul_f32_e32 v68, 0xbfb8aa3b, v84
	v_exp_f32_e32 v68, v68
	v_mul_f32_e32 v2, v2, v80
	v_add_f32_e32 v81, 1.0, v81
	v_rcp_f32_e32 v81, v81
	v_add_f32_e32 v68, 1.0, v68
	v_rcp_f32_e32 v136, v68
	v_xor_b32_e32 v78, 16, v212
	v_mul_f32_e32 v68, v2, v81
	v_mul_f32_e32 v2, v50, v84
	v_cmp_lt_i32_e32 vcc, v78, v83
	v_mul_f32_e32 v50, v2, v136
	v_mul_f32_e32 v80, v50, v50
	v_cndmask_b32_e32 v78, v212, v78, vcc
	v_lshlrev_b32_e32 v78, 2, v78
	v_fmac_f32_e32 v80, v68, v68
	v_mov_b32_e32 v81, v80
	s_nop 1
	v_permlane16_swap_b32_e32 v81, v80
	v_xor_b32_e32 v2, 8, v212
	v_cmp_lt_i32_e32 vcc, v2, v83
	v_add_f32_e32 v81, v80, v81
	v_cndmask_b32_e32 v2, v212, v2, vcc
	v_lshlrev_b32_e32 v2, 2, v2
	s_nop 1
	v_mov_b32_dpp v84, v81 row_ror:8 row_mask:0xf bank_mask:0xf
	v_xor_b32_e32 v80, 4, v212
	v_cmp_lt_i32_e32 vcc, v80, v83
	v_add_f32_e32 v84, v81, v84
	v_cndmask_b32_e32 v80, v212, v80, vcc
	v_lshlrev_b32_e32 v80, 2, v80
	s_nop 1
	v_mov_b32_dpp v136, v84 row_shr:4 row_mask:0xf bank_mask:0xa
	v_mov_b32_dpp v136, v84 row_shl:4 row_mask:0xf bank_mask:0x5
	v_xor_b32_e32 v81, 2, v212
	v_cmp_lt_i32_e32 vcc, v81, v83
	v_add_f32_e32 v136, v84, v136
	v_cndmask_b32_e32 v81, v212, v81, vcc
	v_lshlrev_b32_e32 v81, 2, v81
	s_nop 1
	v_mov_b32_dpp v137, v136 quad_perm:[2,3,0,1] row_mask:0xf bank_mask:0xf
	v_xor_b32_e32 v84, 1, v212
	v_cmp_lt_i32_e32 vcc, v84, v83
	v_add_f32_e32 v136, v136, v137
	v_cndmask_b32_e32 v83, v212, v84, vcc
	v_lshlrev_b32_e32 v84, 2, v83
	s_nop 1
	v_mov_b32_dpp v137, v136 quad_perm:[1,0,3,2] row_mask:0xf bank_mask:0xf
	v_lshl_add_u32 v83, v213, 2, s80
	v_cmp_eq_u32_e32 vcc, 0, v195
	v_add_u32_e32 v83, v83, v214
	s_and_saveexec_b64 s[6:7], vcc
	s_cbranch_execz .LBB0_831
	v_add_f32_e32 v136, v136, v137
	ds_write_b32 v83, v136

.LBB0_1026:
	v_or_b32_e32 v52, s0, v83
	v_ashrrev_i32_e32 v53, 31, v52
	v_lshlrev_b64 v[50:51], 12, v[52:53]
	v_lshl_add_u64 v[2:3], v[72:73], 0, v[50:51]
	global_load_dwordx4 v[88:91], v[2:3], off nt
	global_load_dwordx4 v[96:99], v[2:3], off offset:1024 nt
	global_load_dwordx4 v[236:239], v[2:3], off offset:2048 nt
	global_load_dwordx4 v[240:243], v[2:3], off offset:3072 nt
	v_or_b32_e32 v86, 1, v52
	v_ashrrev_i32_e32 v87, 31, v86
	v_or_b32_e32 v64, 2, v52
	v_lshlrev_b64 v[84:85], 12, v[86:87]
	v_ashrrev_i32_e32 v65, 31, v64
	v_or_b32_e32 v60, 3, v52
	v_lshl_add_u64 v[2:3], v[72:73], 0, v[84:85]
	v_lshlrev_b64 v[62:63], 12, v[64:65]
	v_ashrrev_i32_e32 v61, 31, v60
	global_load_dwordx4 v[46:49], v[2:3], off nt
	global_load_dwordx4 v[42:45], v[2:3], off offset:1024 nt
	global_load_dwordx4 v[38:41], v[2:3], off offset:2048 nt
	global_load_dwordx4 v[34:37], v[2:3], off offset:3072 nt
	v_lshl_add_u64 v[2:3], v[72:73], 0, v[62:63]
	v_lshlrev_b64 v[58:59], 12, v[60:61]
	global_load_dwordx4 v[30:33], v[2:3], off nt
	global_load_dwordx4 v[26:29], v[2:3], off offset:1024 nt
	global_load_dwordx4 v[22:25], v[2:3], off offset:2048 nt
	global_load_dwordx4 v[18:21], v[2:3], off offset:3072 nt
	v_lshl_add_u64 v[2:3], v[72:73], 0, v[58:59]
	global_load_dwordx4 v[14:17], v[2:3], off nt
	global_load_dwordx4 v[10:13], v[2:3], off offset:1024 nt
	global_load_dwordx4 v[6:9], v[2:3], off offset:2048 nt
	s_nop 0
	global_load_dwordx4 v[2:5], v[2:3], off offset:3072 nt
	v_lshlrev_b64 v[52:53], 11, v[52:53]
	s_waitcnt vmcnt(15)
	v_lshlrev_b32_e32 v94, 16, v88
	v_and_b32_e32 v92, 0xffff0000, v88
	v_add_f32_e32 v88, 0, v94
	v_lshlrev_b32_e32 v56, 16, v89
	v_add_f32_e32 v88, v88, v92
	v_and_b32_e32 v54, 0xffff0000, v89
	v_add_f32_e32 v88, v88, v56
	v_lshlrev_b32_e32 v95, 16, v90
	v_add_f32_e32 v88, v88, v54
	v_and_b32_e32 v93, 0xffff0000, v90
	v_add_f32_e32 v88, v88, v95
	v_lshlrev_b32_e32 v57, 16, v91
	v_add_f32_e32 v88, v88, v93
	v_and_b32_e32 v55, 0xffff0000, v91
	v_add_f32_e32 v88, v88, v57
	s_waitcnt vmcnt(14)
	v_lshlrev_b32_e32 v235, 16, v96
	v_add_f32_e32 v88, v88, v55
	v_and_b32_e32 v233, 0xffff0000, v96
	v_add_f32_e32 v88, v88, v235
	v_lshlrev_b32_e32 v231, 16, v97
	v_add_f32_e32 v88, v88, v233
	v_and_b32_e32 v228, 0xffff0000, v97
	v_add_f32_e32 v88, v88, v231
	v_lshlrev_b32_e32 v234, 16, v98
	v_add_f32_e32 v88, v88, v228
	v_and_b32_e32 v232, 0xffff0000, v98
	v_add_f32_e32 v88, v88, v234
	v_lshlrev_b32_e32 v230, 16, v99
	v_add_f32_e32 v88, v88, v232
	v_and_b32_e32 v229, 0xffff0000, v99
	v_add_f32_e32 v88, v88, v230
	s_waitcnt vmcnt(13)
	v_lshlrev_b32_e32 v226, 16, v236
	v_add_f32_e32 v88, v88, v229
	v_and_b32_e32 v224, 0xffff0000, v236
	v_add_f32_e32 v88, v88, v226
	v_lshlrev_b32_e32 v222, 16, v237
	v_add_f32_e32 v88, v88, v224
	v_and_b32_e32 v100, 0xffff0000, v237
	v_add_f32_e32 v88, v88, v222
	v_lshlrev_b32_e32 v227, 16, v238
	v_add_f32_e32 v88, v88, v100
	v_and_b32_e32 v225, 0xffff0000, v238
	v_add_f32_e32 v88, v88, v227
	v_lshlrev_b32_e32 v223, 16, v239
	v_add_f32_e32 v88, v88, v225
	v_and_b32_e32 v101, 0xffff0000, v239
	v_add_f32_e32 v88, v88, v223
	s_waitcnt vmcnt(12)
	v_lshlrev_b32_e32 v99, 16, v240
	v_add_f32_e32 v88, v88, v101
	v_and_b32_e32 v98, 0xffff0000, v240
	v_add_f32_e32 v88, v88, v99
	v_lshlrev_b32_e32 v97, 16, v241
	v_add_f32_e32 v88, v88, v98
	v_and_b32_e32 v96, 0xffff0000, v241
	v_add_f32_e32 v88, v88, v97
	v_add_f32_e32 v122, v88, v96
	v_lshlrev_b32_e32 v91, 16, v242
	v_and_b32_e32 v90, 0xffff0000, v242
	v_add_f32_e32 v122, v122, v91
	v_lshlrev_b32_e32 v89, 16, v243
	v_add_f32_e32 v122, v122, v90
	v_and_b32_e32 v88, 0xffff0000, v243
	v_add_f32_e32 v122, v122, v89
	v_add_f32_e32 v122, v122, v88
	v_mov_b32_e32 v123, v122
	s_nop 1
	v_permlane32_swap_b32_e32 v123, v122
	s_waitcnt lgkmcnt(0)
	v_add_f32_e32 v122, v122, v123
	v_mov_b32_e32 v123, v122
	s_nop 1
	v_permlane16_swap_b32_e32 v123, v122
	s_waitcnt lgkmcnt(0)
	v_add_f32_e32 v122, v122, v123
	s_nop 1
	v_mov_b32_dpp v123, v122 row_ror:8 row_mask:0xf bank_mask:0xf
	s_waitcnt lgkmcnt(0)
	v_add_f32_e32 v122, v122, v123
	s_nop 1
	v_mov_b32_dpp v123, v122 row_shr:4 row_mask:0xf bank_mask:0xa
	v_mov_b32_dpp v123, v122 row_shl:4 row_mask:0xf bank_mask:0x5
	s_waitcnt lgkmcnt(0)
	v_add_f32_e32 v122, v122, v123
	s_nop 1
	v_mov_b32_dpp v123, v122 quad_perm:[2,3,0,1] row_mask:0xf bank_mask:0xf
	s_waitcnt lgkmcnt(0)
	v_add_f32_e32 v122, v122, v123
	s_nop 1
	v_mov_b32_dpp v123, v122 quad_perm:[1,0,3,2] row_mask:0xf bank_mask:0xf
	s_waitcnt lgkmcnt(0)
	v_add_f32_e32 v122, v122, v123
	v_fmamk_f32 v236, v122, 0xba000000, v92
	v_fmamk_f32 v123, v122, 0xba000000, v94
	v_mul_f32_e32 v239, v236, v236
	v_fmac_f32_e32 v239, v123, v123
	v_fmamk_f32 v123, v122, 0xba000000, v56
	v_fmac_f32_e32 v239, v123, v123
	v_fmamk_f32 v123, v122, 0xba000000, v54
	v_fmac_f32_e32 v239, v123, v123
	v_fmamk_f32 v123, v122, 0xba000000, v95
	v_fmac_f32_e32 v239, v123, v123
	v_fmamk_f32 v123, v122, 0xba000000, v93
	v_fmac_f32_e32 v239, v123, v123
	v_fmamk_f32 v123, v122, 0xba000000, v57
	v_fmac_f32_e32 v239, v123, v123
	v_fmamk_f32 v123, v122, 0xba000000, v55
	v_fmac_f32_e32 v239, v123, v123
	v_fmamk_f32 v123, v122, 0xba000000, v235
	v_fmac_f32_e32 v239, v123, v123
	v_fmamk_f32 v123, v122, 0xba000000, v233
	v_fmac_f32_e32 v239, v123, v123
	v_fmamk_f32 v123, v122, 0xba000000, v231
	v_fmac_f32_e32 v239, v123, v123
	v_fmamk_f32 v123, v122, 0xba000000, v228
	v_fmac_f32_e32 v239, v123, v123
	v_fmamk_f32 v123, v122, 0xba000000, v234
	v_fmac_f32_e32 v239, v123, v123
	v_fmamk_f32 v123, v122, 0xba000000, v232
	v_fmac_f32_e32 v239, v123, v123
	v_fmamk_f32 v123, v122, 0xba000000, v230
	v_fmac_f32_e32 v239, v123, v123
	v_fmamk_f32 v123, v122, 0xba000000, v229
	v_fmac_f32_e32 v239, v123, v123
	v_fmamk_f32 v123, v122, 0xba000000, v226
	v_fmac_f32_e32 v239, v123, v123
	v_fmamk_f32 v123, v122, 0xba000000, v224
	v_fmac_f32_e32 v239, v123, v123
	v_fmamk_f32 v123, v122, 0xba000000, v222
	v_fmac_f32_e32 v239, v123, v123
	v_fmamk_f32 v123, v122, 0xba000000, v100
	v_fmac_f32_e32 v239, v123, v123
	v_fmamk_f32 v123, v122, 0xba000000, v227
	v_fmac_f32_e32 v239, v123, v123
	v_fmamk_f32 v123, v122, 0xba000000, v225
	v_fmac_f32_e32 v239, v123, v123
	v_fmamk_f32 v123, v122, 0xba000000, v223
	v_fmac_f32_e32 v239, v123, v123
	v_fmamk_f32 v123, v122, 0xba000000, v101
	v_fmac_f32_e32 v239, v123, v123
	v_fmamk_f32 v123, v122, 0xba000000, v99
	v_fmac_f32_e32 v239, v123, v123
	v_fmamk_f32 v123, v122, 0xba000000, v98
	v_fmac_f32_e32 v239, v123, v123
	v_fmamk_f32 v123, v122, 0xba000000, v97
	v_mul_f32_e32 v238, 0x3a000000, v122
	v_fmac_f32_e32 v239, v123, v123
	v_fmamk_f32 v122, v122, 0xba000000, v96
	v_fmac_f32_e32 v239, v122, v122
	v_pk_add_f32 v[236:237], v[90:91], v[238:239] op_sel_hi:[1,0] neg_lo:[0,1] neg_hi:[0,1]
	s_nop 0
	v_pk_mul_f32 v[236:237], v[236:237], v[236:237]
	s_nop 0
	v_add_f32_e32 v122, v237, v239
	v_add_f32_e32 v122, v236, v122
	v_pk_add_f32 v[236:237], v[88:89], v[238:239] op_sel_hi:[1,0] neg_lo:[0,1] neg_hi:[0,1]
	s_nop 0
	v_pk_mul_f32 v[236:237], v[236:237], v[236:237]
	s_nop 0
	v_add_f32_e32 v122, v237, v122
	v_add_f32_e32 v122, v236, v122
	v_mov_b32_e32 v123, v122
	s_nop 1
	v_permlane32_swap_b32_e32 v123, v122
	s_waitcnt lgkmcnt(0)
	v_add_f32_e32 v122, v122, v123
	v_mov_b32_e32 v123, v122
	s_nop 1
	v_permlane16_swap_b32_e32 v123, v122
	s_waitcnt lgkmcnt(0)
	v_add_f32_e32 v122, v122, v123
	s_nop 1
	v_mov_b32_dpp v123, v122 row_ror:8 row_mask:0xf bank_mask:0xf
	s_waitcnt lgkmcnt(0)
	v_add_f32_e32 v122, v122, v123
	s_nop 1
	v_mov_b32_dpp v123, v122 row_shr:4 row_mask:0xf bank_mask:0xa
	v_mov_b32_dpp v123, v122 row_shl:4 row_mask:0xf bank_mask:0x5
	s_waitcnt lgkmcnt(0)
	v_add_f32_e32 v122, v122, v123
	s_nop 1
	v_mov_b32_dpp v123, v122 quad_perm:[2,3,0,1] row_mask:0xf bank_mask:0xf
	s_waitcnt lgkmcnt(0)
	v_add_f32_e32 v122, v122, v123
	s_nop 1
	v_mov_b32_dpp v123, v122 quad_perm:[1,0,3,2] row_mask:0xf bank_mask:0xf
	s_waitcnt lgkmcnt(0)
	v_add_f32_e32 v122, v122, v123
	v_fmamk_f32 v122, v122, 0x3a000000, v219
	v_cmp_gt_f32_e32 vcc, s33, v122
	v_mul_f32_e32 v123, 0x4b800000, v122
	s_nop 0
	v_cndmask_b32_e32 v122, v122, v123, vcc
	v_rsq_f32_e32 v122, v122
	s_nop 0
	v_mul_f32_e32 v123, 0x45800000, v122
	v_cndmask_b32_e32 v236, v122, v123, vcc
	v_mul_f32_e64 v237, v236, -v238
	ds_read_b128 v[238:241], v112 offset:4096
	ds_read_b128 v[242:245], v112 offset:4112
	ds_read_b128 v[246:249], v112 offset:12288
	ds_read_b128 v[250:253], v112 offset:12304
	v_fma_f32 v94, v94, v236, v237
	v_fma_f32 v92, v92, v236, v237
	v_fma_f32 v93, v93, v236, v237
	s_waitcnt lgkmcnt(1)
	v_fma_f32 v122, v94, v238, v246
	v_fma_f32 v94, v95, v236, v237
	v_fma_f32 v56, v56, v236, v237
	v_fma_f32 v54, v54, v236, v237
	s_waitcnt lgkmcnt(0)
	v_fma_f32 v123, v94, v242, v250
	v_fma_f32 v92, v92, v239, v247
	v_fma_f32 v93, v93, v243, v251
	v_fma_f32 v238, v56, v240, v248
	v_fma_f32 v56, v57, v236, v237
	v_fmac_f32_e32 v249, v54, v241
	v_fma_f32 v54, v55, v236, v237
	v_fma_f32 v239, v56, v244, v252
	v_fmac_f32_e32 v253, v54, v245
	v_cvt_pk_bf16_f32 v54, v122, v92
	v_cvt_pk_bf16_f32 v55, v238, v249
	v_cvt_pk_bf16_f32 v56, v123, v93
	v_cvt_pk_fp8_f32 v122, v122, v92
	v_cvt_pk_fp8_f32 v123, v123, v93
	v_lshl_add_u64 v[94:95], v[76:77], 0, v[50:51]
	v_lshl_add_u64 v[92:93], v[78:79], 0, v[52:53]
	v_cvt_pk_fp8_f32 v122, v238, v249 op_sel:[0,0,1]
	v_cvt_pk_fp8_f32 v123, v239, v253 op_sel:[0,0,1]
	v_cvt_pk_bf16_f32 v57, v239, v253
	global_store_dwordx4 v[94:95], v[54:57], off nt
	v_fma_f32 v99, v99, v236, v237
	global_store_dwordx2 v[92:93], v[122:123], off
	ds_read_b128 v[238:241], v112 offset:6144
	ds_read_b128 v[242:245], v112 offset:6160
	ds_read_b128 v[54:57], v112 offset:14336
	ds_read_b128 v[50:53], v112 offset:14352
	v_fma_f32 v122, v235, v236, v237
	s_waitcnt lgkmcnt(1)
	v_fma_f32 v122, v122, v238, v54
	v_fma_f32 v54, v234, v236, v237
	s_waitcnt lgkmcnt(0)
	v_fma_f32 v123, v54, v242, v50
	v_fma_f32 v50, v233, v236, v237
	v_fma_f32 v50, v50, v239, v55
	v_fma_f32 v54, v232, v236, v237
	v_fma_f32 v55, v230, v236, v237
	v_fma_f32 v51, v54, v243, v51
	v_fma_f32 v54, v231, v236, v237
	v_fma_f32 v52, v55, v244, v52
	v_fma_f32 v55, v228, v236, v237
	v_fma_f32 v54, v54, v240, v56
	v_fmac_f32_e32 v57, v55, v241
	v_fma_f32 v55, v229, v236, v237
	v_cvt_pk_bf16_f32 v228, v122, v50
	v_cvt_pk_bf16_f32 v229, v54, v57
	v_cvt_pk_bf16_f32 v230, v123, v51
	v_cvt_pk_fp8_f32 v122, v122, v50
	v_cvt_pk_fp8_f32 v123, v123, v51
	v_fmac_f32_e32 v53, v55, v245
	v_cvt_pk_bf16_f32 v231, v52, v53
	v_cvt_pk_fp8_f32 v122, v54, v57 op_sel:[0,0,1]
	v_cvt_pk_fp8_f32 v123, v52, v53 op_sel:[0,0,1]
	global_store_dwordx4 v[94:95], v[228:231], off offset:1024 nt
	global_store_dwordx2 v[92:93], v[122:123], off offset:512
	ds_read_b128 v[50:53], v112 offset:8192
	ds_read_b128 v[54:57], v112 offset:8208
	ds_read_b128 v[228:231], v112 offset:16384
	ds_read_b128 v[232:235], v112 offset:16400
	v_fma_f32 v122, v226, v236, v237
	s_waitcnt lgkmcnt(1)
	v_fma_f32 v122, v122, v50, v228
	v_fma_f32 v50, v227, v236, v237
	s_waitcnt lgkmcnt(0)
	v_fma_f32 v123, v50, v54, v232
	v_fma_f32 v50, v224, v236, v237
	v_fma_f32 v54, v50, v51, v229
	v_fma_f32 v50, v225, v236, v237
	v_fma_f32 v55, v50, v55, v233
	v_fma_f32 v50, v222, v236, v237
	v_fma_f32 v222, v50, v52, v230
	v_fma_f32 v50, v223, v236, v237
	v_fma_f32 v56, v50, v56, v234
	v_fma_f32 v50, v100, v236, v237
	v_fmac_f32_e32 v231, v50, v53
	v_fma_f32 v50, v101, v236, v237
	v_fmac_f32_e32 v235, v50, v57
	v_cvt_pk_bf16_f32 v50, v122, v54
	v_cvt_pk_bf16_f32 v51, v222, v231
	v_cvt_pk_bf16_f32 v52, v123, v55
	v_cvt_pk_fp8_f32 v122, v122, v54
	v_cvt_pk_fp8_f32 v123, v123, v55
	v_cvt_pk_bf16_f32 v53, v56, v235
	global_store_dwordx4 v[94:95], v[50:53], off offset:2048 nt
	v_cvt_pk_fp8_f32 v122, v222, v231 op_sel:[0,0,1]
	v_cvt_pk_fp8_f32 v123, v56, v235 op_sel:[0,0,1]
	global_store_dwordx2 v[92:93], v[122:123], off offset:1024
	ds_read_b128 v[50:53], v112 offset:10240
	ds_read_b128 v[54:57], v112 offset:10256
	ds_read_b128 v[222:225], v112 offset:18432
	ds_read_b128 v[226:229], v112 offset:18448
	s_waitcnt lgkmcnt(1)
	v_fma_f32 v100, v99, v50, v222
	v_fma_f32 v50, v91, v236, v237
	s_waitcnt lgkmcnt(0)
	v_fma_f32 v101, v50, v54, v226
	v_fma_f32 v50, v98, v236, v237
	v_fma_f32 v54, v50, v51, v223
	v_fma_f32 v50, v90, v236, v237
	v_fma_f32 v55, v50, v55, v227
	v_fma_f32 v50, v97, v236, v237
	v_fma_f32 v90, v50, v52, v224
	v_fma_f32 v50, v89, v236, v237
	v_fma_f32 v56, v50, v56, v228
	v_fma_f32 v50, v96, v236, v237
	v_fmac_f32_e32 v225, v50, v53
	v_cvt_pk_bf16_f32 v50, v100, v54
	v_cvt_pk_bf16_f32 v51, v90, v225
	v_cvt_pk_bf16_f32 v52, v101, v55
	v_cvt_pk_fp8_f32 v100, v100, v54
	v_cvt_pk_fp8_f32 v101, v101, v55
	v_fmac_f32_e32 v237, v88, v236
	v_fmac_f32_e32 v229, v237, v57
	v_cvt_pk_fp8_f32 v100, v90, v225 op_sel:[0,0,1]
	v_cvt_pk_fp8_f32 v101, v56, v229 op_sel:[0,0,1]
	v_cvt_pk_bf16_f32 v53, v56, v229
	global_store_dwordx4 v[94:95], v[50:53], off offset:3072 nt
	global_store_dwordx2 v[92:93], v[100:101], off offset:1536
	s_waitcnt vmcnt(19)
	v_lshlrev_b32_e32 v56, 16, v46
	v_and_b32_e32 v88, 0xffff0000, v46
	s_waitcnt vmcnt(16)
	v_lshlrev_b32_e32 v228, 16, v34
	v_and_b32_e32 v229, 0xffff0000, v34
	v_add_f32_e32 v34, 0, v56
	v_lshlrev_b32_e32 v89, 16, v47
	v_add_f32_e32 v34, v34, v88
	v_and_b32_e32 v90, 0xffff0000, v47
	v_add_f32_e32 v34, v34, v89
	v_lshlrev_b32_e32 v57, 16, v48
	v_add_f32_e32 v34, v34, v90
	v_and_b32_e32 v91, 0xffff0000, v48
	v_add_f32_e32 v34, v34, v57
	v_lshlrev_b32_e32 v92, 16, v49
	v_add_f32_e32 v34, v34, v91
	v_and_b32_e32 v93, 0xffff0000, v49
	v_add_f32_e32 v34, v34, v92
	v_lshlrev_b32_e32 v94, 16, v42
	v_add_f32_e32 v34, v34, v93
	v_and_b32_e32 v95, 0xffff0000, v42
	v_add_f32_e32 v34, v34, v94
	v_lshlrev_b32_e32 v96, 16, v43
	v_add_f32_e32 v34, v34, v95
	v_and_b32_e32 v97, 0xffff0000, v43
	v_add_f32_e32 v34, v34, v96
	v_lshlrev_b32_e32 v98, 16, v44
	v_add_f32_e32 v34, v34, v97
	v_and_b32_e32 v99, 0xffff0000, v44
	v_add_f32_e32 v34, v34, v98
	v_lshlrev_b32_e32 v100, 16, v45
	v_add_f32_e32 v34, v34, v99
	v_and_b32_e32 v101, 0xffff0000, v45
	v_add_f32_e32 v34, v34, v100
	v_lshlrev_b32_e32 v122, 16, v38
	v_add_f32_e32 v34, v34, v101
	v_and_b32_e32 v123, 0xffff0000, v38
	v_add_f32_e32 v34, v34, v122
	v_lshlrev_b32_e32 v222, 16, v39
	v_add_f32_e32 v34, v34, v123
	v_and_b32_e32 v223, 0xffff0000, v39
	v_add_f32_e32 v34, v34, v222
	v_lshlrev_b32_e32 v224, 16, v40
	v_add_f32_e32 v34, v34, v223
	v_and_b32_e32 v225, 0xffff0000, v40
	v_add_f32_e32 v34, v34, v224
	v_lshlrev_b32_e32 v226, 16, v41
	v_add_f32_e32 v34, v34, v225
	v_and_b32_e32 v227, 0xffff0000, v41
	v_add_f32_e32 v34, v34, v226
	v_add_f32_e32 v34, v34, v227
	v_add_f32_e32 v34, v34, v228
	v_lshlrev_b32_e32 v230, 16, v35
	v_add_f32_e32 v34, v34, v229
	v_and_b32_e32 v231, 0xffff0000, v35
	v_add_f32_e32 v34, v34, v230
	v_add_f32_e32 v40, v34, v231
	v_lshlrev_b32_e32 v39, 16, v36
	v_and_b32_e32 v38, 0xffff0000, v36
	v_add_f32_e32 v36, v40, v39
	v_lshlrev_b32_e32 v35, 16, v37
	v_add_f32_e32 v36, v36, v38
	v_and_b32_e32 v34, 0xffff0000, v37
	v_add_f32_e32 v36, v36, v35
	v_add_f32_e32 v36, v36, v34
	v_mov_b32_e32 v37, v36
	s_nop 1
	v_permlane32_swap_b32_e32 v37, v36
	v_lshl_add_u64 v[84:85], v[76:77], 0, v[84:85]
	s_waitcnt lgkmcnt(0)
	v_add_f32_e32 v36, v36, v37
	v_mov_b32_e32 v37, v36
	s_nop 1
	v_permlane16_swap_b32_e32 v37, v36
	s_waitcnt lgkmcnt(0)
	v_add_f32_e32 v36, v36, v37
	s_nop 1
	v_mov_b32_dpp v37, v36 row_ror:8 row_mask:0xf bank_mask:0xf
	s_waitcnt lgkmcnt(0)
	v_add_f32_e32 v36, v36, v37
	s_nop 1
	v_mov_b32_dpp v37, v36 row_shr:4 row_mask:0xf bank_mask:0xa
	v_mov_b32_dpp v37, v36 row_shl:4 row_mask:0xf bank_mask:0x5
	s_waitcnt lgkmcnt(0)
	v_add_f32_e32 v36, v36, v37
	s_nop 1
	v_mov_b32_dpp v37, v36 quad_perm:[2,3,0,1] row_mask:0xf bank_mask:0xf
	s_waitcnt lgkmcnt(0)
	v_add_f32_e32 v36, v36, v37
	s_nop 1
	v_mov_b32_dpp v37, v36 quad_perm:[1,0,3,2] row_mask:0xf bank_mask:0xf
	s_waitcnt lgkmcnt(0)
	v_add_f32_e32 v37, v36, v37
	v_fmamk_f32 v41, v37, 0xba000000, v88
	v_fmamk_f32 v40, v37, 0xba000000, v56
	v_mul_f32_e32 v42, v41, v41
	v_fmac_f32_e32 v42, v40, v40
	v_fmamk_f32 v40, v37, 0xba000000, v89
	v_fmac_f32_e32 v42, v40, v40
	v_fmamk_f32 v40, v37, 0xba000000, v90
	v_fmac_f32_e32 v42, v40, v40
	v_fmamk_f32 v40, v37, 0xba000000, v57
	v_fmac_f32_e32 v42, v40, v40
	v_fmamk_f32 v40, v37, 0xba000000, v91
	v_fmac_f32_e32 v42, v40, v40
	v_fmamk_f32 v40, v37, 0xba000000, v92
	v_fmac_f32_e32 v42, v40, v40
	v_fmamk_f32 v40, v37, 0xba000000, v93
	v_fmac_f32_e32 v42, v40, v40
	v_fmamk_f32 v40, v37, 0xba000000, v94
	v_fmac_f32_e32 v42, v40, v40
	v_fmamk_f32 v40, v37, 0xba000000, v95
	v_fmac_f32_e32 v42, v40, v40
	v_fmamk_f32 v40, v37, 0xba000000, v96
	v_fmac_f32_e32 v42, v40, v40
	v_fmamk_f32 v40, v37, 0xba000000, v97
	v_fmac_f32_e32 v42, v40, v40
	v_fmamk_f32 v40, v37, 0xba000000, v98
	v_fmac_f32_e32 v42, v40, v40
	v_fmamk_f32 v40, v37, 0xba000000, v99
	v_fmac_f32_e32 v42, v40, v40
	v_fmamk_f32 v40, v37, 0xba000000, v100
	v_fmac_f32_e32 v42, v40, v40
	v_fmamk_f32 v40, v37, 0xba000000, v101
	v_fmac_f32_e32 v42, v40, v40
	v_fmamk_f32 v40, v37, 0xba000000, v122
	v_fmac_f32_e32 v42, v40, v40
	v_fmamk_f32 v40, v37, 0xba000000, v123
	v_fmac_f32_e32 v42, v40, v40
	v_fmamk_f32 v40, v37, 0xba000000, v222
	v_fmac_f32_e32 v42, v40, v40
	v_fmamk_f32 v40, v37, 0xba000000, v223
	v_fmac_f32_e32 v42, v40, v40
	v_fmamk_f32 v40, v37, 0xba000000, v224
	v_fmac_f32_e32 v42, v40, v40
	v_fmamk_f32 v40, v37, 0xba000000, v225
	v_fmac_f32_e32 v42, v40, v40
	v_fmamk_f32 v40, v37, 0xba000000, v226
	v_fmac_f32_e32 v42, v40, v40
	v_fmamk_f32 v40, v37, 0xba000000, v227
	v_fmac_f32_e32 v42, v40, v40
	v_fmamk_f32 v40, v37, 0xba000000, v228
	v_fmac_f32_e32 v42, v40, v40
	v_fmamk_f32 v40, v37, 0xba000000, v229
	v_mul_f32_e32 v36, 0x3a000000, v37
	v_fmac_f32_e32 v42, v40, v40
	v_fmamk_f32 v40, v37, 0xba000000, v230
	v_fmamk_f32 v37, v37, 0xba000000, v231
	v_fmac_f32_e32 v42, v40, v40
	v_pk_add_f32 v[40:41], v[38:39], v[36:37] op_sel_hi:[1,0] neg_lo:[0,1] neg_hi:[0,1]
	v_fmac_f32_e32 v42, v37, v37
	v_pk_mul_f32 v[40:41], v[40:41], v[40:41]
	s_nop 0
	v_add_f32_e32 v37, v41, v42
	v_add_f32_e32 v37, v40, v37
	v_pk_add_f32 v[40:41], v[34:35], v[36:37] op_sel_hi:[1,0] neg_lo:[0,1] neg_hi:[0,1]
	s_nop 0
	v_pk_mul_f32 v[40:41], v[40:41], v[40:41]
	s_nop 0
	v_add_f32_e32 v37, v41, v37
	v_add_f32_e32 v37, v40, v37
	v_mov_b32_e32 v40, v37
	s_nop 1
	v_permlane32_swap_b32_e32 v40, v37
	s_waitcnt lgkmcnt(0)
	v_add_f32_e32 v37, v37, v40
	v_mov_b32_e32 v40, v37
	s_nop 1
	v_permlane16_swap_b32_e32 v40, v37
	s_waitcnt lgkmcnt(0)
	v_add_f32_e32 v37, v37, v40
	s_nop 1
	v_mov_b32_dpp v40, v37 row_ror:8 row_mask:0xf bank_mask:0xf
	s_waitcnt lgkmcnt(0)
	v_add_f32_e32 v37, v37, v40
	s_nop 1
	v_mov_b32_dpp v40, v37 row_shr:4 row_mask:0xf bank_mask:0xa
	v_mov_b32_dpp v40, v37 row_shl:4 row_mask:0xf bank_mask:0x5
	s_waitcnt lgkmcnt(0)
	v_add_f32_e32 v37, v37, v40
	s_nop 1
	v_mov_b32_dpp v40, v37 quad_perm:[2,3,0,1] row_mask:0xf bank_mask:0xf
	s_waitcnt lgkmcnt(0)
	v_add_f32_e32 v37, v37, v40
	s_nop 1
	v_mov_b32_dpp v40, v37 quad_perm:[1,0,3,2] row_mask:0xf bank_mask:0xf
	s_waitcnt lgkmcnt(0)
	v_add_f32_e32 v37, v37, v40
	v_fmamk_f32 v37, v37, 0x3a000000, v219
	v_mul_f32_e32 v40, 0x4b800000, v37
	v_cmp_gt_f32_e32 vcc, s33, v37
	s_nop 1
	v_cndmask_b32_e32 v37, v37, v40, vcc
	v_rsq_f32_e32 v37, v37
	s_nop 0
	v_mul_f32_e32 v40, 0x45800000, v37
	v_cndmask_b32_e32 v232, v37, v40, vcc
	ds_read_b128 v[40:43], v112 offset:12288
	ds_read_b128 v[44:47], v112 offset:4096
	ds_read_b128 v[48:51], v112 offset:4112
	ds_read_b128 v[52:55], v112 offset:12304
	v_mul_f32_e64 v233, v232, -v36
	v_fma_f32 v56, v56, v232, v233
	s_waitcnt lgkmcnt(2)
	v_fma_f32 v56, v56, v44, v40
	v_fma_f32 v40, v57, v232, v233
	v_fma_f32 v44, v89, v232, v233
	s_waitcnt lgkmcnt(0)
	v_fma_f32 v57, v40, v48, v52
	v_fma_f32 v40, v88, v232, v233
	v_fma_f32 v42, v44, v46, v42
	v_fma_f32 v44, v92, v232, v233
	v_fma_f32 v40, v40, v45, v41
	v_fma_f32 v41, v91, v232, v233
	v_fma_f32 v48, v44, v50, v54
	v_fma_f32 v44, v90, v232, v233
	v_fma_f32 v41, v41, v49, v53
	v_fmac_f32_e32 v43, v44, v47
	v_fma_f32 v44, v93, v232, v233
	v_fmac_f32_e32 v55, v44, v51
	v_cvt_pk_bf16_f32 v44, v56, v40
	v_cvt_pk_bf16_f32 v45, v42, v43
	v_cvt_pk_bf16_f32 v46, v57, v41
	v_cvt_pk_fp8_f32 v56, v56, v40
	v_cvt_pk_fp8_f32 v57, v57, v41
	v_cvt_pk_bf16_f32 v47, v48, v55
	global_store_dwordx4 v[84:85], v[44:47], off nt
	v_cvt_pk_fp8_f32 v56, v42, v43 op_sel:[0,0,1]
	v_cvt_pk_fp8_f32 v57, v48, v55 op_sel:[0,0,1]
	ds_read_b128 v[40:43], v112 offset:14336
	ds_read_b128 v[44:47], v112 offset:6144
	ds_read_b128 v[48:51], v112 offset:6160
	ds_read_b128 v[52:55], v112 offset:14352
	v_lshlrev_b64 v[36:37], 11, v[86:87]
	v_lshl_add_u64 v[86:87], v[78:79], 0, v[36:37]
	v_fma_f32 v36, v94, v232, v233
	s_waitcnt lgkmcnt(2)
	v_fma_f32 v36, v36, v44, v40
	v_fma_f32 v44, v96, v232, v233
	v_fma_f32 v37, v98, v232, v233
	v_fma_f32 v40, v95, v232, v233
	v_fma_f32 v42, v44, v46, v42
	v_fma_f32 v44, v100, v232, v233
	s_waitcnt lgkmcnt(0)
	v_fma_f32 v37, v37, v48, v52
	v_fma_f32 v40, v40, v45, v41
	v_fma_f32 v41, v99, v232, v233
	v_fma_f32 v48, v44, v50, v54
	v_fma_f32 v44, v97, v232, v233
	v_fma_f32 v41, v41, v49, v53
	v_fmac_f32_e32 v43, v44, v47
	v_fma_f32 v44, v101, v232, v233
	global_store_dwordx2 v[86:87], v[56:57], off
	v_fmac_f32_e32 v55, v44, v51
	v_cvt_pk_bf16_f32 v44, v36, v40
	v_cvt_pk_bf16_f32 v45, v42, v43
	v_cvt_pk_bf16_f32 v46, v37, v41
	v_cvt_pk_fp8_f32 v36, v36, v40
	v_cvt_pk_fp8_f32 v37, v37, v41
	v_cvt_pk_bf16_f32 v47, v48, v55
	global_store_dwordx4 v[84:85], v[44:47], off offset:1024 nt
	v_cvt_pk_fp8_f32 v36, v42, v43 op_sel:[0,0,1]
	v_cvt_pk_fp8_f32 v37, v48, v55 op_sel:[0,0,1]
	ds_read_b128 v[40:43], v112 offset:16384
	ds_read_b128 v[44:47], v112 offset:8192
	ds_read_b128 v[48:51], v112 offset:8208
	ds_read_b128 v[52:55], v112 offset:16400
	v_fma_f32 v35, v35, v232, v233
	global_store_dwordx2 v[86:87], v[36:37], off offset:512
	v_fma_f32 v36, v122, v232, v233
	s_waitcnt lgkmcnt(2)
	v_fma_f32 v36, v36, v44, v40
	v_fma_f32 v44, v222, v232, v233
	v_fma_f32 v37, v224, v232, v233
	v_fma_f32 v40, v123, v232, v233
	v_fma_f32 v42, v44, v46, v42
	v_fma_f32 v44, v226, v232, v233
	s_waitcnt lgkmcnt(0)
	v_fma_f32 v37, v37, v48, v52
	v_fma_f32 v40, v40, v45, v41
	v_fma_f32 v41, v225, v232, v233
	v_fma_f32 v48, v44, v50, v54
	v_fma_f32 v44, v223, v232, v233
	v_fma_f32 v41, v41, v49, v53
	v_fmac_f32_e32 v43, v44, v47
	v_fma_f32 v44, v227, v232, v233
	v_fmac_f32_e32 v55, v44, v51
	v_cvt_pk_bf16_f32 v44, v36, v40
	v_cvt_pk_bf16_f32 v45, v42, v43
	v_cvt_pk_bf16_f32 v46, v37, v41
	v_cvt_pk_fp8_f32 v36, v36, v40
	v_cvt_pk_fp8_f32 v37, v37, v41
	v_cvt_pk_bf16_f32 v47, v48, v55
	global_store_dwordx4 v[84:85], v[44:47], off offset:2048 nt
	v_cvt_pk_fp8_f32 v36, v42, v43 op_sel:[0,0,1]
	v_cvt_pk_fp8_f32 v37, v48, v55 op_sel:[0,0,1]
	ds_read_b128 v[40:43], v112 offset:18432
	ds_read_b128 v[44:47], v112 offset:10240
	ds_read_b128 v[48:51], v112 offset:10256
	ds_read_b128 v[52:55], v112 offset:18448
	global_store_dwordx2 v[86:87], v[36:37], off offset:1024
	v_fma_f32 v36, v228, v232, v233
	s_waitcnt lgkmcnt(2)
	v_fma_f32 v56, v36, v44, v40
	v_fma_f32 v36, v39, v232, v233
	s_waitcnt lgkmcnt(0)
	v_fma_f32 v57, v36, v48, v52
	v_fma_f32 v36, v229, v232, v233
	v_fma_f32 v39, v36, v45, v41
	v_fma_f32 v36, v38, v232, v233
	v_fma_f32 v40, v36, v49, v53
	v_fma_f32 v36, v230, v232, v233
	v_fma_f32 v41, v36, v46, v42
	v_fma_f32 v36, v231, v232, v233
	v_fmac_f32_e32 v43, v36, v47
	v_cvt_pk_bf16_f32 v36, v56, v39
	v_cvt_pk_bf16_f32 v37, v41, v43
	v_cvt_pk_bf16_f32 v38, v57, v40
	v_cvt_pk_fp8_f32 v56, v56, v39
	v_cvt_pk_fp8_f32 v57, v57, v40
	v_fmac_f32_e32 v233, v34, v232
	v_fma_f32 v35, v35, v50, v54
	v_fmac_f32_e32 v55, v233, v51
	v_cvt_pk_fp8_f32 v56, v41, v43 op_sel:[0,0,1]
	v_cvt_pk_fp8_f32 v57, v35, v55 op_sel:[0,0,1]
	v_cvt_pk_bf16_f32 v39, v35, v55
	global_store_dwordx4 v[84:85], v[36:39], off offset:3072 nt
	global_store_dwordx2 v[86:87], v[56:57], off offset:1536
	s_waitcnt vmcnt(23)
	v_lshlrev_b32_e32 v40, 16, v30
	v_and_b32_e32 v42, 0xffff0000, v30
	s_waitcnt vmcnt(20)
	v_lshlrev_b32_e32 v90, 16, v18
	v_and_b32_e32 v91, 0xffff0000, v18
	v_add_f32_e32 v18, 0, v40
	v_lshlrev_b32_e32 v43, 16, v31
	v_add_f32_e32 v18, v18, v42
	v_and_b32_e32 v44, 0xffff0000, v31
	v_add_f32_e32 v18, v18, v43
	v_lshlrev_b32_e32 v41, 16, v32
	v_add_f32_e32 v18, v18, v44
	v_and_b32_e32 v45, 0xffff0000, v32
	v_add_f32_e32 v18, v18, v41
	v_lshlrev_b32_e32 v46, 16, v33
	v_add_f32_e32 v18, v18, v45
	v_and_b32_e32 v47, 0xffff0000, v33
	v_add_f32_e32 v18, v18, v46
	v_lshlrev_b32_e32 v48, 16, v26
	v_add_f32_e32 v18, v18, v47
	v_and_b32_e32 v49, 0xffff0000, v26
	v_add_f32_e32 v18, v18, v48
	v_lshlrev_b32_e32 v50, 16, v27
	v_add_f32_e32 v18, v18, v49
	v_and_b32_e32 v51, 0xffff0000, v27
	v_add_f32_e32 v18, v18, v50
	v_lshlrev_b32_e32 v52, 16, v28
	v_add_f32_e32 v18, v18, v51
	v_and_b32_e32 v53, 0xffff0000, v28
	v_add_f32_e32 v18, v18, v52
	v_lshlrev_b32_e32 v54, 16, v29
	v_add_f32_e32 v18, v18, v53
	v_and_b32_e32 v55, 0xffff0000, v29
	v_add_f32_e32 v18, v18, v54
	v_lshlrev_b32_e32 v56, 16, v22
	v_add_f32_e32 v18, v18, v55
	v_and_b32_e32 v57, 0xffff0000, v22
	v_add_f32_e32 v18, v18, v56
	v_lshlrev_b32_e32 v84, 16, v23
	v_add_f32_e32 v18, v18, v57
	v_and_b32_e32 v85, 0xffff0000, v23
	v_add_f32_e32 v18, v18, v84
	v_lshlrev_b32_e32 v86, 16, v24
	v_add_f32_e32 v18, v18, v85
	v_and_b32_e32 v87, 0xffff0000, v24
	v_add_f32_e32 v18, v18, v86
	v_lshlrev_b32_e32 v88, 16, v25
	v_add_f32_e32 v18, v18, v87
	v_and_b32_e32 v89, 0xffff0000, v25
	v_add_f32_e32 v18, v18, v88
	v_add_f32_e32 v18, v18, v89
	v_add_f32_e32 v18, v18, v90
	v_lshlrev_b32_e32 v92, 16, v19
	v_add_f32_e32 v18, v18, v91
	v_and_b32_e32 v93, 0xffff0000, v19
	v_add_f32_e32 v18, v18, v92
	v_add_f32_e32 v24, v18, v93
	v_lshlrev_b32_e32 v23, 16, v20
	v_and_b32_e32 v22, 0xffff0000, v20
	v_add_f32_e32 v20, v24, v23
	v_lshlrev_b32_e32 v19, 16, v21
	v_add_f32_e32 v20, v20, v22
	v_and_b32_e32 v18, 0xffff0000, v21
	v_add_f32_e32 v20, v20, v19
	v_add_f32_e32 v20, v20, v18
	v_mov_b32_e32 v21, v20
	s_nop 1
	v_permlane32_swap_b32_e32 v21, v20
	s_waitcnt lgkmcnt(0)
	v_add_f32_e32 v20, v20, v21
	v_mov_b32_e32 v21, v20
	s_nop 1
	v_permlane16_swap_b32_e32 v21, v20
	s_waitcnt lgkmcnt(0)
	v_add_f32_e32 v20, v20, v21
	s_nop 1
	v_mov_b32_dpp v21, v20 row_ror:8 row_mask:0xf bank_mask:0xf
	s_waitcnt lgkmcnt(0)
	v_add_f32_e32 v20, v20, v21
	s_nop 1
	v_mov_b32_dpp v21, v20 row_shr:4 row_mask:0xf bank_mask:0xa
	v_mov_b32_dpp v21, v20 row_shl:4 row_mask:0xf bank_mask:0x5
	s_waitcnt lgkmcnt(0)
	v_add_f32_e32 v20, v20, v21
	s_nop 1
	v_mov_b32_dpp v21, v20 quad_perm:[2,3,0,1] row_mask:0xf bank_mask:0xf
	s_waitcnt lgkmcnt(0)
	v_add_f32_e32 v20, v20, v21
	s_nop 1
	v_mov_b32_dpp v21, v20 quad_perm:[1,0,3,2] row_mask:0xf bank_mask:0xf
	s_waitcnt lgkmcnt(0)
	v_add_f32_e32 v21, v20, v21
	v_fmamk_f32 v25, v21, 0xba000000, v42
	v_fmamk_f32 v24, v21, 0xba000000, v40
	v_mul_f32_e32 v26, v25, v25
	v_fmac_f32_e32 v26, v24, v24
	v_fmamk_f32 v24, v21, 0xba000000, v43
	v_fmac_f32_e32 v26, v24, v24
	v_fmamk_f32 v24, v21, 0xba000000, v44
	v_fmac_f32_e32 v26, v24, v24
	v_fmamk_f32 v24, v21, 0xba000000, v41
	v_fmac_f32_e32 v26, v24, v24
	v_fmamk_f32 v24, v21, 0xba000000, v45
	v_fmac_f32_e32 v26, v24, v24
	v_fmamk_f32 v24, v21, 0xba000000, v46
	v_fmac_f32_e32 v26, v24, v24
	v_fmamk_f32 v24, v21, 0xba000000, v47
	v_fmac_f32_e32 v26, v24, v24
	v_fmamk_f32 v24, v21, 0xba000000, v48
	v_fmac_f32_e32 v26, v24, v24
	v_fmamk_f32 v24, v21, 0xba000000, v49
	v_fmac_f32_e32 v26, v24, v24
	v_fmamk_f32 v24, v21, 0xba000000, v50
	v_fmac_f32_e32 v26, v24, v24
	v_fmamk_f32 v24, v21, 0xba000000, v51
	v_fmac_f32_e32 v26, v24, v24
	v_fmamk_f32 v24, v21, 0xba000000, v52
	v_fmac_f32_e32 v26, v24, v24
	v_fmamk_f32 v24, v21, 0xba000000, v53
	v_fmac_f32_e32 v26, v24, v24
	v_fmamk_f32 v24, v21, 0xba000000, v54
	v_fmac_f32_e32 v26, v24, v24
	v_fmamk_f32 v24, v21, 0xba000000, v55
	v_fmac_f32_e32 v26, v24, v24
	v_fmamk_f32 v24, v21, 0xba000000, v56
	v_fmac_f32_e32 v26, v24, v24
	v_fmamk_f32 v24, v21, 0xba000000, v57
	v_fmac_f32_e32 v26, v24, v24
	v_fmamk_f32 v24, v21, 0xba000000, v84
	v_fmac_f32_e32 v26, v24, v24
	v_fmamk_f32 v24, v21, 0xba000000, v85
	v_fmac_f32_e32 v26, v24, v24
	v_fmamk_f32 v24, v21, 0xba000000, v86
	v_fmac_f32_e32 v26, v24, v24
	v_fmamk_f32 v24, v21, 0xba000000, v87
	v_fmac_f32_e32 v26, v24, v24
	v_fmamk_f32 v24, v21, 0xba000000, v88
	v_fmac_f32_e32 v26, v24, v24
	v_fmamk_f32 v24, v21, 0xba000000, v89
	v_fmac_f32_e32 v26, v24, v24
	v_fmamk_f32 v24, v21, 0xba000000, v90
	v_fmac_f32_e32 v26, v24, v24
	v_fmamk_f32 v24, v21, 0xba000000, v91
	v_mul_f32_e32 v20, 0x3a000000, v21
	v_fmac_f32_e32 v26, v24, v24
	v_fmamk_f32 v24, v21, 0xba000000, v92
	v_fmamk_f32 v21, v21, 0xba000000, v93
	v_fmac_f32_e32 v26, v24, v24
	v_pk_add_f32 v[24:25], v[22:23], v[20:21] op_sel_hi:[1,0] neg_lo:[0,1] neg_hi:[0,1]
	v_fmac_f32_e32 v26, v21, v21
	v_pk_mul_f32 v[24:25], v[24:25], v[24:25]
	s_nop 0
	v_add_f32_e32 v21, v25, v26
	v_add_f32_e32 v21, v24, v21
	v_pk_add_f32 v[24:25], v[18:19], v[20:21] op_sel_hi:[1,0] neg_lo:[0,1] neg_hi:[0,1]
	s_nop 0
	v_pk_mul_f32 v[24:25], v[24:25], v[24:25]
	s_nop 0
	v_add_f32_e32 v21, v25, v21
	v_add_f32_e32 v21, v24, v21
	v_mov_b32_e32 v24, v21
	s_nop 1
	v_permlane32_swap_b32_e32 v24, v21
	s_waitcnt lgkmcnt(0)
	v_add_f32_e32 v21, v21, v24
	v_mov_b32_e32 v24, v21
	s_nop 1
	v_permlane16_swap_b32_e32 v24, v21
	s_waitcnt lgkmcnt(0)
	v_add_f32_e32 v21, v21, v24
	s_nop 1
	v_mov_b32_dpp v24, v21 row_ror:8 row_mask:0xf bank_mask:0xf
	s_waitcnt lgkmcnt(0)
	v_add_f32_e32 v21, v21, v24
	s_nop 1
	v_mov_b32_dpp v24, v21 row_shr:4 row_mask:0xf bank_mask:0xa
	v_mov_b32_dpp v24, v21 row_shl:4 row_mask:0xf bank_mask:0x5
	s_waitcnt lgkmcnt(0)
	v_add_f32_e32 v21, v21, v24
	s_nop 1
	v_mov_b32_dpp v24, v21 quad_perm:[2,3,0,1] row_mask:0xf bank_mask:0xf
	s_waitcnt lgkmcnt(0)
	v_add_f32_e32 v21, v21, v24
	s_nop 1
	v_mov_b32_dpp v24, v21 quad_perm:[1,0,3,2] row_mask:0xf bank_mask:0xf
	s_waitcnt lgkmcnt(0)
	v_add_f32_e32 v21, v21, v24
	v_fmamk_f32 v21, v21, 0x3a000000, v219
	v_mul_f32_e32 v24, 0x4b800000, v21
	v_cmp_gt_f32_e32 vcc, s33, v21
	s_nop 1
	v_cndmask_b32_e32 v21, v21, v24, vcc
	v_rsq_f32_e32 v21, v21
	s_nop 0
	v_mul_f32_e32 v24, 0x45800000, v21
	v_cndmask_b32_e32 v94, v21, v24, vcc
	ds_read_b128 v[24:27], v112 offset:12288
	ds_read_b128 v[28:31], v112 offset:4096
	ds_read_b128 v[32:35], v112 offset:4112
	ds_read_b128 v[36:39], v112 offset:12304
	v_mul_f32_e64 v95, v94, -v20
	v_fma_f32 v40, v40, v94, v95
	s_waitcnt lgkmcnt(2)
	v_fma_f32 v40, v40, v28, v24
	v_fma_f32 v24, v41, v94, v95
	v_fma_f32 v28, v43, v94, v95
	s_waitcnt lgkmcnt(0)
	v_fma_f32 v41, v24, v32, v36
	v_fma_f32 v24, v42, v94, v95
	v_fma_f32 v26, v28, v30, v26
	v_fma_f32 v28, v46, v94, v95
	v_fma_f32 v24, v24, v29, v25
	v_fma_f32 v25, v45, v94, v95
	v_fma_f32 v32, v28, v34, v38
	v_fma_f32 v28, v44, v94, v95
	v_fma_f32 v25, v25, v33, v37
	v_fmac_f32_e32 v27, v28, v31
	v_fma_f32 v28, v47, v94, v95
	v_fmac_f32_e32 v39, v28, v35
	v_cvt_pk_bf16_f32 v28, v40, v24
	v_cvt_pk_bf16_f32 v29, v26, v27
	v_cvt_pk_bf16_f32 v30, v41, v25
	v_cvt_pk_fp8_f32 v40, v40, v24
	v_cvt_pk_fp8_f32 v41, v41, v25
	v_lshl_add_u64 v[42:43], v[76:77], 0, v[62:63]
	v_cvt_pk_bf16_f32 v31, v32, v39
	global_store_dwordx4 v[42:43], v[28:31], off nt
	v_cvt_pk_fp8_f32 v40, v26, v27 op_sel:[0,0,1]
	v_cvt_pk_fp8_f32 v41, v32, v39 op_sel:[0,0,1]
	ds_read_b128 v[24:27], v112 offset:14336
	ds_read_b128 v[28:31], v112 offset:6144
	ds_read_b128 v[32:35], v112 offset:6160
	ds_read_b128 v[36:39], v112 offset:14352
	v_lshlrev_b64 v[20:21], 11, v[64:65]
	v_lshl_add_u64 v[44:45], v[78:79], 0, v[20:21]
	v_fma_f32 v20, v48, v94, v95
	s_waitcnt lgkmcnt(2)
	v_fma_f32 v20, v20, v28, v24
	v_fma_f32 v28, v50, v94, v95
	v_fma_f32 v21, v52, v94, v95
	v_fma_f32 v24, v49, v94, v95
	v_fma_f32 v26, v28, v30, v26
	v_fma_f32 v28, v54, v94, v95
	s_waitcnt lgkmcnt(0)
	v_fma_f32 v21, v21, v32, v36
	v_fma_f32 v24, v24, v29, v25
	v_fma_f32 v25, v53, v94, v95
	v_fma_f32 v32, v28, v34, v38
	v_fma_f32 v28, v51, v94, v95
	v_fma_f32 v25, v25, v33, v37
	v_fmac_f32_e32 v27, v28, v31
	v_fma_f32 v28, v55, v94, v95
	global_store_dwordx2 v[44:45], v[40:41], off
	v_fmac_f32_e32 v39, v28, v35
	v_cvt_pk_bf16_f32 v28, v20, v24
	v_cvt_pk_bf16_f32 v29, v26, v27
	v_cvt_pk_bf16_f32 v30, v21, v25
	v_cvt_pk_fp8_f32 v20, v20, v24
	v_cvt_pk_fp8_f32 v21, v21, v25
	v_cvt_pk_bf16_f32 v31, v32, v39
	global_store_dwordx4 v[42:43], v[28:31], off offset:1024 nt
	v_cvt_pk_fp8_f32 v20, v26, v27 op_sel:[0,0,1]
	v_cvt_pk_fp8_f32 v21, v32, v39 op_sel:[0,0,1]
	ds_read_b128 v[24:27], v112 offset:16384
	ds_read_b128 v[28:31], v112 offset:8192
	ds_read_b128 v[32:35], v112 offset:8208
	ds_read_b128 v[36:39], v112 offset:16400
	v_fma_f32 v19, v19, v94, v95
	global_store_dwordx2 v[44:45], v[20:21], off offset:512
	v_fma_f32 v20, v56, v94, v95
	s_waitcnt lgkmcnt(2)
	v_fma_f32 v20, v20, v28, v24
	v_fma_f32 v28, v84, v94, v95
	v_fma_f32 v21, v86, v94, v95
	v_fma_f32 v24, v57, v94, v95
	v_fma_f32 v26, v28, v30, v26
	v_fma_f32 v28, v88, v94, v95
	s_waitcnt lgkmcnt(0)
	v_fma_f32 v21, v21, v32, v36
	v_fma_f32 v24, v24, v29, v25
	v_fma_f32 v25, v87, v94, v95
	v_fma_f32 v32, v28, v34, v38
	v_fma_f32 v28, v85, v94, v95
	v_fma_f32 v25, v25, v33, v37
	v_fmac_f32_e32 v27, v28, v31
	v_fma_f32 v28, v89, v94, v95
	v_fmac_f32_e32 v39, v28, v35
	v_cvt_pk_bf16_f32 v28, v20, v24
	v_cvt_pk_bf16_f32 v29, v26, v27
	v_cvt_pk_bf16_f32 v30, v21, v25
	v_cvt_pk_fp8_f32 v20, v20, v24
	v_cvt_pk_fp8_f32 v21, v21, v25
	v_cvt_pk_bf16_f32 v31, v32, v39
	global_store_dwordx4 v[42:43], v[28:31], off offset:2048 nt
	v_cvt_pk_fp8_f32 v20, v26, v27 op_sel:[0,0,1]
	v_cvt_pk_fp8_f32 v21, v32, v39 op_sel:[0,0,1]
	ds_read_b128 v[24:27], v112 offset:18432
	ds_read_b128 v[28:31], v112 offset:10240
	ds_read_b128 v[32:35], v112 offset:10256
	ds_read_b128 v[36:39], v112 offset:18448
	global_store_dwordx2 v[44:45], v[20:21], off offset:1024
	v_fma_f32 v20, v90, v94, v95
	s_waitcnt lgkmcnt(2)
	v_fma_f32 v40, v20, v28, v24
	v_fma_f32 v20, v23, v94, v95
	s_waitcnt lgkmcnt(0)
	v_fma_f32 v41, v20, v32, v36
	v_fma_f32 v20, v91, v94, v95
	v_fma_f32 v23, v20, v29, v25
	v_fma_f32 v20, v22, v94, v95
	v_fma_f32 v24, v20, v33, v37
	v_fma_f32 v20, v92, v94, v95
	v_fma_f32 v25, v20, v30, v26
	v_fma_f32 v20, v93, v94, v95
	v_fmac_f32_e32 v27, v20, v31
	v_cvt_pk_bf16_f32 v20, v40, v23
	v_cvt_pk_bf16_f32 v21, v25, v27
	v_cvt_pk_bf16_f32 v22, v41, v24
	v_cvt_pk_fp8_f32 v40, v40, v23
	v_cvt_pk_fp8_f32 v41, v41, v24
	v_fmac_f32_e32 v95, v18, v94
	v_fma_f32 v19, v19, v34, v38
	v_fmac_f32_e32 v39, v95, v35
	v_cvt_pk_fp8_f32 v40, v25, v27 op_sel:[0,0,1]
	v_cvt_pk_fp8_f32 v41, v19, v39 op_sel:[0,0,1]
	v_cvt_pk_bf16_f32 v23, v19, v39
	global_store_dwordx4 v[42:43], v[20:23], off offset:3072 nt
	global_store_dwordx2 v[44:45], v[40:41], off offset:1536
	s_waitcnt vmcnt(27)
	v_lshlrev_b32_e32 v24, 16, v14
	v_and_b32_e32 v26, 0xffff0000, v14
	s_waitcnt vmcnt(24)
	v_lshlrev_b32_e32 v48, 16, v2
	v_and_b32_e32 v49, 0xffff0000, v2
	v_add_f32_e32 v2, 0, v24
	v_lshlrev_b32_e32 v27, 16, v15
	v_add_f32_e32 v2, v2, v26
	v_and_b32_e32 v28, 0xffff0000, v15
	v_add_f32_e32 v2, v2, v27
	v_lshlrev_b32_e32 v25, 16, v16
	v_add_f32_e32 v2, v2, v28
	v_and_b32_e32 v29, 0xffff0000, v16
	v_add_f32_e32 v2, v2, v25
	v_lshlrev_b32_e32 v30, 16, v17
	v_add_f32_e32 v2, v2, v29
	v_and_b32_e32 v31, 0xffff0000, v17
	v_add_f32_e32 v2, v2, v30
	v_lshlrev_b32_e32 v32, 16, v10
	v_add_f32_e32 v2, v2, v31
	v_and_b32_e32 v33, 0xffff0000, v10
	v_add_f32_e32 v2, v2, v32
	v_lshlrev_b32_e32 v34, 16, v11
	v_add_f32_e32 v2, v2, v33
	v_and_b32_e32 v35, 0xffff0000, v11
	v_add_f32_e32 v2, v2, v34
	v_lshlrev_b32_e32 v36, 16, v12
	v_add_f32_e32 v2, v2, v35
	v_and_b32_e32 v37, 0xffff0000, v12
	v_add_f32_e32 v2, v2, v36
	v_lshlrev_b32_e32 v38, 16, v13
	v_add_f32_e32 v2, v2, v37
	v_and_b32_e32 v39, 0xffff0000, v13
	v_add_f32_e32 v2, v2, v38
	v_lshlrev_b32_e32 v40, 16, v6
	v_add_f32_e32 v2, v2, v39
	v_and_b32_e32 v41, 0xffff0000, v6
	v_add_f32_e32 v2, v2, v40
	v_lshlrev_b32_e32 v42, 16, v7
	v_add_f32_e32 v2, v2, v41
	v_and_b32_e32 v43, 0xffff0000, v7
	v_add_f32_e32 v2, v2, v42
	v_lshlrev_b32_e32 v44, 16, v8
	v_add_f32_e32 v2, v2, v43
	v_and_b32_e32 v45, 0xffff0000, v8
	v_add_f32_e32 v2, v2, v44
	v_lshlrev_b32_e32 v46, 16, v9
	v_add_f32_e32 v2, v2, v45
	v_and_b32_e32 v47, 0xffff0000, v9
	v_add_f32_e32 v2, v2, v46
	v_add_f32_e32 v2, v2, v47
	v_add_f32_e32 v2, v2, v48
	v_lshlrev_b32_e32 v50, 16, v3
	v_add_f32_e32 v2, v2, v49
	v_and_b32_e32 v51, 0xffff0000, v3
	v_add_f32_e32 v2, v2, v50
	v_add_f32_e32 v8, v2, v51
	v_lshlrev_b32_e32 v7, 16, v4
	v_and_b32_e32 v6, 0xffff0000, v4
	v_add_f32_e32 v4, v8, v7
	v_lshlrev_b32_e32 v3, 16, v5
	v_add_f32_e32 v4, v4, v6
	v_and_b32_e32 v2, 0xffff0000, v5
	v_add_f32_e32 v4, v4, v3
	v_add_f32_e32 v4, v4, v2
	v_mov_b32_e32 v5, v4
	s_nop 1
	v_permlane32_swap_b32_e32 v5, v4
	s_waitcnt lgkmcnt(0)
	v_add_f32_e32 v4, v4, v5
	v_mov_b32_e32 v5, v4
	s_nop 1
	v_permlane16_swap_b32_e32 v5, v4
	s_waitcnt lgkmcnt(0)
	v_add_f32_e32 v4, v4, v5
	s_nop 1
	v_mov_b32_dpp v5, v4 row_ror:8 row_mask:0xf bank_mask:0xf
	s_waitcnt lgkmcnt(0)
	v_add_f32_e32 v4, v4, v5
	s_nop 1
	v_mov_b32_dpp v5, v4 row_shr:4 row_mask:0xf bank_mask:0xa
	v_mov_b32_dpp v5, v4 row_shl:4 row_mask:0xf bank_mask:0x5
	s_waitcnt lgkmcnt(0)
	v_add_f32_e32 v4, v4, v5
	s_nop 1
	v_mov_b32_dpp v5, v4 quad_perm:[2,3,0,1] row_mask:0xf bank_mask:0xf
	s_waitcnt lgkmcnt(0)
	v_add_f32_e32 v4, v4, v5
	s_nop 1
	v_mov_b32_dpp v5, v4 quad_perm:[1,0,3,2] row_mask:0xf bank_mask:0xf
	s_waitcnt lgkmcnt(0)
	v_add_f32_e32 v5, v4, v5
	v_fmamk_f32 v9, v5, 0xba000000, v26
	v_fmamk_f32 v8, v5, 0xba000000, v24
	v_mul_f32_e32 v10, v9, v9
	v_fmac_f32_e32 v10, v8, v8
	v_fmamk_f32 v8, v5, 0xba000000, v27
	v_fmac_f32_e32 v10, v8, v8
	v_fmamk_f32 v8, v5, 0xba000000, v28
	v_fmac_f32_e32 v10, v8, v8
	v_fmamk_f32 v8, v5, 0xba000000, v25
	v_fmac_f32_e32 v10, v8, v8
	v_fmamk_f32 v8, v5, 0xba000000, v29
	v_fmac_f32_e32 v10, v8, v8
	v_fmamk_f32 v8, v5, 0xba000000, v30
	v_fmac_f32_e32 v10, v8, v8
	v_fmamk_f32 v8, v5, 0xba000000, v31
	v_fmac_f32_e32 v10, v8, v8
	v_fmamk_f32 v8, v5, 0xba000000, v32
	v_fmac_f32_e32 v10, v8, v8
	v_fmamk_f32 v8, v5, 0xba000000, v33
	v_fmac_f32_e32 v10, v8, v8
	v_fmamk_f32 v8, v5, 0xba000000, v34
	v_fmac_f32_e32 v10, v8, v8
	v_fmamk_f32 v8, v5, 0xba000000, v35
	v_fmac_f32_e32 v10, v8, v8
	v_fmamk_f32 v8, v5, 0xba000000, v36
	v_fmac_f32_e32 v10, v8, v8
	v_fmamk_f32 v8, v5, 0xba000000, v37
	v_fmac_f32_e32 v10, v8, v8
	v_fmamk_f32 v8, v5, 0xba000000, v38
	v_fmac_f32_e32 v10, v8, v8
	v_fmamk_f32 v8, v5, 0xba000000, v39
	v_fmac_f32_e32 v10, v8, v8
	v_fmamk_f32 v8, v5, 0xba000000, v40
	v_fmac_f32_e32 v10, v8, v8
	v_fmamk_f32 v8, v5, 0xba000000, v41
	v_fmac_f32_e32 v10, v8, v8
	v_fmamk_f32 v8, v5, 0xba000000, v42
	v_fmac_f32_e32 v10, v8, v8
	v_fmamk_f32 v8, v5, 0xba000000, v43
	v_fmac_f32_e32 v10, v8, v8
	v_fmamk_f32 v8, v5, 0xba000000, v44
	v_fmac_f32_e32 v10, v8, v8
	v_fmamk_f32 v8, v5, 0xba000000, v45
	v_fmac_f32_e32 v10, v8, v8
	v_fmamk_f32 v8, v5, 0xba000000, v46
	v_fmac_f32_e32 v10, v8, v8
	v_fmamk_f32 v8, v5, 0xba000000, v47
	v_fmac_f32_e32 v10, v8, v8
	v_fmamk_f32 v8, v5, 0xba000000, v48
	v_fmac_f32_e32 v10, v8, v8
	v_fmamk_f32 v8, v5, 0xba000000, v49
	v_mul_f32_e32 v4, 0x3a000000, v5
	v_fmac_f32_e32 v10, v8, v8
	v_fmamk_f32 v8, v5, 0xba000000, v50
	v_fmamk_f32 v5, v5, 0xba000000, v51
	v_fmac_f32_e32 v10, v8, v8
	v_pk_add_f32 v[8:9], v[6:7], v[4:5] op_sel_hi:[1,0] neg_lo:[0,1] neg_hi:[0,1]
	v_fmac_f32_e32 v10, v5, v5
	v_pk_mul_f32 v[8:9], v[8:9], v[8:9]
	s_nop 0
	v_add_f32_e32 v5, v9, v10
	v_add_f32_e32 v5, v8, v5
	v_pk_add_f32 v[8:9], v[2:3], v[4:5] op_sel_hi:[1,0] neg_lo:[0,1] neg_hi:[0,1]
	s_nop 0
	v_pk_mul_f32 v[8:9], v[8:9], v[8:9]
	s_nop 0
	v_add_f32_e32 v5, v9, v5
	v_add_f32_e32 v5, v8, v5
	v_mov_b32_e32 v8, v5
	s_nop 1
	v_permlane32_swap_b32_e32 v8, v5
	s_waitcnt lgkmcnt(0)
	v_add_f32_e32 v5, v5, v8
	v_mov_b32_e32 v8, v5
	s_nop 1
	v_permlane16_swap_b32_e32 v8, v5
	s_waitcnt lgkmcnt(0)
	v_add_f32_e32 v5, v5, v8
	s_nop 1
	v_mov_b32_dpp v8, v5 row_ror:8 row_mask:0xf bank_mask:0xf
	s_waitcnt lgkmcnt(0)
	v_add_f32_e32 v5, v5, v8
	s_nop 1
	v_mov_b32_dpp v8, v5 row_shr:4 row_mask:0xf bank_mask:0xa
	v_mov_b32_dpp v8, v5 row_shl:4 row_mask:0xf bank_mask:0x5
	s_waitcnt lgkmcnt(0)
	v_add_f32_e32 v5, v5, v8
	s_nop 1
	v_mov_b32_dpp v8, v5 quad_perm:[2,3,0,1] row_mask:0xf bank_mask:0xf
	s_waitcnt lgkmcnt(0)
	v_add_f32_e32 v5, v5, v8
	s_nop 1
	v_mov_b32_dpp v8, v5 quad_perm:[1,0,3,2] row_mask:0xf bank_mask:0xf
	s_waitcnt lgkmcnt(0)
	v_add_f32_e32 v5, v5, v8
	v_fmamk_f32 v5, v5, 0x3a000000, v219
	v_mul_f32_e32 v8, 0x4b800000, v5
	v_cmp_gt_f32_e32 vcc, s33, v5
	s_nop 1
	v_cndmask_b32_e32 v5, v5, v8, vcc
	v_rsq_f32_e32 v5, v5
	s_nop 0
	v_mul_f32_e32 v8, 0x45800000, v5
	v_cndmask_b32_e32 v52, v5, v8, vcc
	ds_read_b128 v[8:11], v112 offset:12288
	ds_read_b128 v[12:15], v112 offset:4096
	ds_read_b128 v[16:19], v112 offset:4112
	ds_read_b128 v[20:23], v112 offset:12304
	v_mul_f32_e64 v53, v52, -v4
	v_fma_f32 v24, v24, v52, v53
	s_waitcnt lgkmcnt(2)
	v_fma_f32 v24, v24, v12, v8
	v_fma_f32 v8, v25, v52, v53
	v_fma_f32 v12, v27, v52, v53
	s_waitcnt lgkmcnt(0)
	v_fma_f32 v25, v8, v16, v20
	v_fma_f32 v8, v26, v52, v53
	v_fma_f32 v10, v12, v14, v10
	v_fma_f32 v12, v30, v52, v53
	v_fma_f32 v8, v8, v13, v9
	v_fma_f32 v9, v29, v52, v53
	v_fma_f32 v16, v12, v18, v22
	v_fma_f32 v12, v28, v52, v53
	v_fma_f32 v9, v9, v17, v21
	v_fmac_f32_e32 v11, v12, v15
	v_fma_f32 v12, v31, v52, v53
	v_fmac_f32_e32 v23, v12, v19
	v_cvt_pk_bf16_f32 v12, v24, v8
	v_cvt_pk_bf16_f32 v13, v10, v11
	v_cvt_pk_bf16_f32 v14, v25, v9
	v_cvt_pk_fp8_f32 v24, v24, v8
	v_cvt_pk_fp8_f32 v25, v25, v9
	v_lshl_add_u64 v[26:27], v[76:77], 0, v[58:59]
	v_cvt_pk_bf16_f32 v15, v16, v23
	global_store_dwordx4 v[26:27], v[12:15], off nt
	v_cvt_pk_fp8_f32 v24, v10, v11 op_sel:[0,0,1]
	v_cvt_pk_fp8_f32 v25, v16, v23 op_sel:[0,0,1]
	ds_read_b128 v[8:11], v112 offset:14336
	ds_read_b128 v[12:15], v112 offset:6144
	ds_read_b128 v[16:19], v112 offset:6160
	ds_read_b128 v[20:23], v112 offset:14352
	v_lshlrev_b64 v[4:5], 11, v[60:61]
	v_lshl_add_u64 v[28:29], v[78:79], 0, v[4:5]
	v_fma_f32 v4, v32, v52, v53
	s_waitcnt lgkmcnt(2)
	v_fma_f32 v4, v4, v12, v8
	v_fma_f32 v12, v34, v52, v53
	v_fma_f32 v5, v36, v52, v53
	v_fma_f32 v8, v33, v52, v53
	v_fma_f32 v10, v12, v14, v10
	v_fma_f32 v12, v38, v52, v53
	s_waitcnt lgkmcnt(0)
	v_fma_f32 v5, v5, v16, v20
	v_fma_f32 v8, v8, v13, v9
	v_fma_f32 v9, v37, v52, v53
	v_fma_f32 v16, v12, v18, v22
	v_fma_f32 v12, v35, v52, v53
	v_fma_f32 v9, v9, v17, v21
	v_fmac_f32_e32 v11, v12, v15
	v_fma_f32 v12, v39, v52, v53
	global_store_dwordx2 v[28:29], v[24:25], off
	v_fmac_f32_e32 v23, v12, v19
	v_cvt_pk_bf16_f32 v12, v4, v8
	v_cvt_pk_bf16_f32 v13, v10, v11
	v_cvt_pk_bf16_f32 v14, v5, v9
	v_cvt_pk_fp8_f32 v4, v4, v8
	v_cvt_pk_fp8_f32 v5, v5, v9
	v_cvt_pk_bf16_f32 v15, v16, v23
	global_store_dwordx4 v[26:27], v[12:15], off offset:1024 nt
	v_cvt_pk_fp8_f32 v4, v10, v11 op_sel:[0,0,1]
	v_cvt_pk_fp8_f32 v5, v16, v23 op_sel:[0,0,1]
	ds_read_b128 v[8:11], v112 offset:16384
	ds_read_b128 v[12:15], v112 offset:8192
	ds_read_b128 v[16:19], v112 offset:8208
	ds_read_b128 v[20:23], v112 offset:16400
	v_fma_f32 v3, v3, v52, v53
	global_store_dwordx2 v[28:29], v[4:5], off offset:512
	v_fma_f32 v4, v40, v52, v53
	s_waitcnt lgkmcnt(2)
	v_fma_f32 v4, v4, v12, v8
	v_fma_f32 v12, v42, v52, v53
	v_fma_f32 v5, v44, v52, v53
	v_fma_f32 v8, v41, v52, v53
	v_fma_f32 v10, v12, v14, v10
	v_fma_f32 v12, v46, v52, v53
	s_waitcnt lgkmcnt(0)
	v_fma_f32 v5, v5, v16, v20
	v_fma_f32 v8, v8, v13, v9
	v_fma_f32 v9, v45, v52, v53
	v_fma_f32 v16, v12, v18, v22
	v_fma_f32 v12, v43, v52, v53
	v_fma_f32 v9, v9, v17, v21
	v_fmac_f32_e32 v11, v12, v15
	v_fma_f32 v12, v47, v52, v53
	v_fmac_f32_e32 v23, v12, v19
	v_cvt_pk_bf16_f32 v12, v4, v8
	v_cvt_pk_bf16_f32 v13, v10, v11
	v_cvt_pk_bf16_f32 v14, v5, v9
	v_cvt_pk_fp8_f32 v4, v4, v8
	v_cvt_pk_fp8_f32 v5, v5, v9
	v_cvt_pk_bf16_f32 v15, v16, v23
	global_store_dwordx4 v[26:27], v[12:15], off offset:2048 nt
	v_cvt_pk_fp8_f32 v4, v10, v11 op_sel:[0,0,1]
	v_cvt_pk_fp8_f32 v5, v16, v23 op_sel:[0,0,1]
	ds_read_b128 v[8:11], v112 offset:18432
	ds_read_b128 v[12:15], v112 offset:10240
	ds_read_b128 v[16:19], v112 offset:10256
	ds_read_b128 v[20:23], v112 offset:18448
	global_store_dwordx2 v[28:29], v[4:5], off offset:1024
	v_fma_f32 v4, v48, v52, v53
	s_waitcnt lgkmcnt(2)
	v_fma_f32 v24, v4, v12, v8
	v_fma_f32 v4, v7, v52, v53
	s_waitcnt lgkmcnt(0)
	v_fma_f32 v25, v4, v16, v20
	v_fma_f32 v4, v49, v52, v53
	v_fma_f32 v7, v4, v13, v9
	v_fma_f32 v4, v6, v52, v53
	v_fma_f32 v8, v4, v17, v21
	v_fma_f32 v4, v50, v52, v53
	v_fma_f32 v9, v4, v14, v10
	v_fma_f32 v4, v51, v52, v53
	v_fmac_f32_e32 v11, v4, v15
	v_cvt_pk_bf16_f32 v4, v24, v7
	v_cvt_pk_bf16_f32 v5, v9, v11
	v_cvt_pk_bf16_f32 v6, v25, v8
	v_cvt_pk_fp8_f32 v24, v24, v7
	v_cvt_pk_fp8_f32 v25, v25, v8
	v_fmac_f32_e32 v53, v2, v52
	v_fma_f32 v3, v3, v18, v22
	v_fmac_f32_e32 v23, v53, v19
	v_cvt_pk_fp8_f32 v24, v9, v11 op_sel:[0,0,1]
	v_cvt_pk_fp8_f32 v25, v3, v23 op_sel:[0,0,1]
	v_cvt_pk_bf16_f32 v7, v3, v23
	global_store_dwordx4 v[26:27], v[4:7], off offset:3072 nt
	global_store_dwordx2 v[28:29], v[24:25], off offset:1536
	s_mov_b32 s0, 4
	s_andn2_b64 vcc, exec, s[26:27]
	s_mov_b64 s[26:27], 0
	s_cbranch_vccz .LBB0_1026
	v_ashrrev_i32_e32 v83, 31, v82
	s_waitcnt vmcnt(0)
	v_lshlrev_b64 v[2:3], 12, v[82:83]
	v_mov_b32_e32 v30, 0
	v_lshl_add_u64 v[84:85], v[80:81], 0, v[2:3]
	s_mov_b64 s[42:43], 0
	v_mov_b32_e32 v31, v30
	v_mov_b32_e32 v32, v30
	v_mov_b32_e32 v33, v30
	v_mov_b32_e32 v6, v30
	v_mov_b32_e32 v7, v30
	v_mov_b32_e32 v8, v30
	v_mov_b32_e32 v9, v30
	v_mov_b32_e32 v14, v30
	v_mov_b32_e32 v15, v30
	v_mov_b32_e32 v16, v30
	v_mov_b32_e32 v17, v30
	v_mov_b32_e32 v26, v30
	v_mov_b32_e32 v27, v30
	v_mov_b32_e32 v28, v30
	v_mov_b32_e32 v29, v30
	v_mov_b32_e32 v2, v30
	v_mov_b32_e32 v3, v30
	v_mov_b32_e32 v4, v30
	v_mov_b32_e32 v5, v30
	v_mov_b32_e32 v10, v30
	v_mov_b32_e32 v11, v30
	v_mov_b32_e32 v12, v30
	v_mov_b32_e32 v13, v30
	v_mov_b32_e32 v18, v30
	v_mov_b32_e32 v19, v30
	v_mov_b32_e32 v20, v30
	v_mov_b32_e32 v21, v30
	v_mov_b32_e32 v34, v30
	v_mov_b32_e32 v35, v30
	v_mov_b32_e32 v36, v30
	v_mov_b32_e32 v37, v30
	v_mov_b32_e32 v38, v30
	v_mov_b32_e32 v39, v30
	v_mov_b32_e32 v40, v30
	v_mov_b32_e32 v41, v30
	v_mov_b32_e32 v42, v30
	v_mov_b32_e32 v43, v30
	v_mov_b32_e32 v44, v30
	v_mov_b32_e32 v45, v30
	v_mov_b32_e32 v46, v30
	v_mov_b32_e32 v47, v30
	v_mov_b32_e32 v48, v30
	v_mov_b32_e32 v49, v30
	v_mov_b32_e32 v50, v30
	v_mov_b32_e32 v51, v30
	v_mov_b32_e32 v52, v30
	v_mov_b32_e32 v53, v30
	v_mov_b32_e32 v54, v30
	v_mov_b32_e32 v55, v30
	v_mov_b32_e32 v56, v30
	v_mov_b32_e32 v57, v30
	v_mov_b32_e32 v58, v30
	v_mov_b32_e32 v59, v30
	v_mov_b32_e32 v60, v30
	v_mov_b32_e32 v61, v30
	v_mov_b32_e32 v62, v30
	v_mov_b32_e32 v63, v30
	v_mov_b32_e32 v64, v30
	v_mov_b32_e32 v65, v30
	v_mov_b32_e32 v22, v30
	v_mov_b32_e32 v23, v30
	v_mov_b32_e32 v24, v30
	v_mov_b32_e32 v25, v30
	s_barrier
